# out-proj phase: tile order permuted so that an XCD owns a contiguous range of row tiles with all 8 column tiles each
# speedup vs baseline: 1.0203x; 1.0098x over previous
; __device__ __forceinline__ void ph_outproj_mfma(const Ctx& c, int layer, int tile, unsigned char* lds) {
;     int mt = tile >> 3; const int nt = tile & 7;
;     if (layer == 1) { if (mt >= 128) return; mt = (mt >> 5) * 34 + 2 + (mt & 31); }
; __global__ void __launch_bounds__(NTHR, 2) mk_fwd(Params prm) {
;     ...
;             case 5: for (int t = bid; t < 136 * 8; t += G) ph_outproj_mfma(c, layer, t, smem_raw); break;
.LBB0_249:
	v_readlane_b32 s16, v254, 2
	v_readlane_b32 s15, v254, 3
	v_readlane_b32 s6, v251, 3
	s_add_i32 s16, s16, s3
	s_add_i32 s15, s15, s6
	s_cmpk_gt_i32 s16, 0x43f
	s_cbranch_scc1 .LBB0_295
.LBB0_250:
	v_writelane_b32 v254, s16, 2
	v_writelane_b32 v254, s15, 3
	s_movk_i32 s28, 0x88
	s_cmp_lg_u64 s[42:43], 0
	s_cselect_b32 s28, 0x80, s28
	s_lshl_b32 s6, s28, 3
	s_cmp_lt_u32 s16, s6
	s_cbranch_scc0 .Lop_noperm
	s_and_b32 s6, s16, 7
	s_lshr_b32 s7, s16, 3
	s_mul_i32 s6, s6, s28
	s_add_i32 s16, s6, s7
	s_lshl_b32 s15, s16, 7
